# nt (streaming) hint on the chunk-A / scan / chunk-C output stores
# baseline (speedup 1.0000x reference)
.LBB0_620:
	s_mov_b64 s[60:61], 0
	s_cbranch_execz .LBB0_642
	s_andn2_b64 vcc, exec, s[30:31]
	s_cbranch_vccnz .LBB0_625
	v_add_u32_e32 v0, s66, v50
	v_ashrrev_i32_e32 v1, 31, v0
	s_load_dwordx4 s[68:71], s[0:1], 0x20
	v_lshlrev_b64 v[0:1], 9, v[0:1]
	v_lshl_add_u64 v[0:1], s[12:13], 0, v[0:1]
	s_lshl_b32 s4, s96, 2
	v_lshl_add_u64 v[0:1], v[0:1], 0, s[4:5]
	s_or_b32 s4, s96, s79
	s_lshl_b64 s[58:59], s[4:5], 2
	s_waitcnt lgkmcnt(0)
	s_add_u32 s62, s68, s58
	s_addc_u32 s63, s69, s59
	s_add_u32 s58, s70, s58
	s_addc_u32 s59, s71, s59
	global_load_dword v2, v[0:1], off
	global_load_dword v3, v137, s[62:63]
	s_nop 0
	global_load_dword v0, v[0:1], off offset:16
	s_mov_b32 s4, 0xbfb8aa3b
	global_load_dword v1, v137, s[58:59]
	s_waitcnt vmcnt(2)
	v_add_f32_e32 v2, v2, v3
	s_waitcnt vmcnt(0)
	v_add_f32_e32 v0, v0, v1
	v_min_f32_e32 v1, 0, v0
	v_mul_f32_e64 v0, |v0|, s4
	v_exp_f32_e32 v0, v0
	s_mov_b32 s4, 0x800000
	v_add_f32_e32 v0, 1.0, v0
	v_cmp_gt_f32_e32 vcc, s4, v0
	s_mov_b32 s4, 0x3f317217
	s_nop 0
	v_cndmask_b32_e64 v4, 0, 32, vcc
	v_ldexp_f32 v0, v0, v4
	v_log_f32_e32 v0, v0
	s_nop 0
	v_mul_f32_e32 v4, 0x3f317217, v0
	v_fma_f32 v4, v0, s4, -v4
	v_fmac_f32_e32 v4, 0x3377d1cf, v0
	v_fmac_f32_e32 v4, 0x3f317217, v0
	v_cmp_lt_f32_e64 s[58:59], |v0|, s36
	s_nop 1
	v_cndmask_b32_e64 v0, v0, v4, s[58:59]
	v_cndmask_b32_e32 v4, 0, v199, vcc
	v_sub_f32_e32 v0, v0, v4
	v_sub_f32_e32 v0, v1, v0
	v_and_b32_e32 v1, 64, v195
	v_add_u32_e32 v4, -1, v195
	v_cmp_lt_i32_e32 vcc, v4, v1
	s_nop 1
	v_cndmask_b32_e32 v4, v4, v195, vcc
	v_lshlrev_b32_e32 v4, 2, v4
	ds_bpermute_b32 v4, v4, v0
	s_waitcnt lgkmcnt(0)
	v_add_f32_e32 v4, v0, v4
	v_cndmask_b32_e64 v0, v4, v0, s[46:47]
	v_add_u32_e32 v4, -2, v195
	v_cmp_lt_i32_e32 vcc, v4, v1
	s_nop 1
	v_cndmask_b32_e32 v4, v4, v195, vcc
	v_lshlrev_b32_e32 v4, 2, v4
	ds_bpermute_b32 v4, v4, v0
	s_waitcnt lgkmcnt(0)
	v_add_f32_e32 v4, v0, v4
	v_cndmask_b32_e64 v0, v4, v0, s[48:49]
	v_add_u32_e32 v4, -4, v195
	v_cmp_lt_i32_e32 vcc, v4, v1
	s_nop 1
	v_cndmask_b32_e32 v4, v4, v195, vcc
	v_lshlrev_b32_e32 v4, 2, v4
	ds_bpermute_b32 v4, v4, v0
	s_waitcnt lgkmcnt(0)
	v_add_f32_e32 v4, v0, v4
	v_cndmask_b32_e64 v0, v4, v0, s[50:51]
	v_add_u32_e32 v4, -8, v195
	v_cmp_lt_i32_e32 vcc, v4, v1
	s_nop 1
	v_cndmask_b32_e32 v4, v4, v195, vcc
	v_lshlrev_b32_e32 v4, 2, v4
	ds_bpermute_b32 v4, v4, v0
	s_waitcnt lgkmcnt(0)
	v_add_f32_e32 v4, v0, v4
	v_cndmask_b32_e64 v0, v4, v0, s[52:53]
	v_add_u32_e32 v4, -16, v195
	v_cmp_lt_i32_e32 vcc, v4, v1
	s_nop 1
	v_cndmask_b32_e32 v4, v4, v195, vcc
	v_lshlrev_b32_e32 v4, 2, v4
	ds_bpermute_b32 v4, v4, v0
	s_waitcnt lgkmcnt(0)
	v_add_f32_e32 v4, v0, v4
	v_cndmask_b32_e64 v0, v4, v0, s[54:55]
	v_subrev_u32_e32 v4, 32, v195
	v_cmp_lt_i32_e32 vcc, v4, v1
	v_add_u32_e32 v1, 64, v1
	s_nop 0
	v_cndmask_b32_e32 v4, v4, v195, vcc
	v_lshlrev_b32_e32 v4, 2, v4
	ds_bpermute_b32 v4, v4, v0
	s_waitcnt lgkmcnt(0)
	v_add_f32_e32 v4, v0, v4
	v_cndmask_b32_e64 v4, v4, v0, s[56:57]
	v_bfrev_b32_e32 v0, 0.5
	v_lshl_or_b32 v0, v195, 2, v0
	ds_bpermute_b32 v0, v0, v4
	s_waitcnt lgkmcnt(0)
	v_sub_f32_e32 v3, v0, v4
	v_add_f32_e32 v2, v2, v3
	v_xor_b32_e32 v3, 1, v195
	v_cmp_lt_i32_e32 vcc, v3, v1
	v_xor_b32_e32 v4, 2, v195
	s_nop 0
	v_cndmask_b32_e32 v3, v195, v3, vcc
	v_lshlrev_b32_e32 v3, 2, v3
	ds_bpermute_b32 v3, v3, v2
	v_cmp_lt_i32_e32 vcc, v4, v1
	s_waitcnt lgkmcnt(0)
	v_max_f32_e32 v3, v3, v3
	v_cndmask_b32_e32 v4, v195, v4, vcc
	v_max_f32_e32 v3, v2, v3
	v_lshlrev_b32_e32 v4, 2, v4
	ds_bpermute_b32 v4, v4, v3
	s_waitcnt lgkmcnt(0)
	v_max_f32_e32 v4, v4, v4
	v_max_f32_e32 v3, v3, v4
	v_xor_b32_e32 v4, 4, v195
	v_cmp_lt_i32_e32 vcc, v4, v1
	s_nop 1
	v_cndmask_b32_e32 v4, v195, v4, vcc
	v_lshlrev_b32_e32 v4, 2, v4
	ds_bpermute_b32 v4, v4, v3
	s_waitcnt lgkmcnt(0)
	v_max_f32_e32 v4, v4, v4
	v_max_f32_e32 v3, v3, v4
	v_xor_b32_e32 v4, 8, v195
	v_cmp_lt_i32_e32 vcc, v4, v1
	s_nop 1
	v_cndmask_b32_e32 v4, v195, v4, vcc
	v_lshlrev_b32_e32 v4, 2, v4
	ds_bpermute_b32 v4, v4, v3
	s_waitcnt lgkmcnt(0)
	v_max_f32_e32 v4, v4, v4
	v_max_f32_e32 v3, v3, v4
	v_xor_b32_e32 v4, 16, v195
	v_cmp_lt_i32_e32 vcc, v4, v1
	s_nop 1
	v_cndmask_b32_e32 v4, v195, v4, vcc
	v_lshlrev_b32_e32 v4, 2, v4
	ds_bpermute_b32 v4, v4, v3
	s_waitcnt lgkmcnt(0)
	v_max_f32_e32 v4, v4, v4
	v_max_f32_e32 v3, v3, v4
	v_xor_b32_e32 v4, 32, v195
	v_cmp_lt_i32_e32 vcc, v4, v1
	s_nop 1
	v_cndmask_b32_e32 v1, v195, v4, vcc
	v_lshlrev_b32_e32 v1, 2, v1
	ds_bpermute_b32 v1, v1, v3
	s_waitcnt lgkmcnt(0)
	v_max_f32_e32 v1, v1, v1
	v_max_f32_e32 v1, v3, v1
	v_sub_f32_e32 v2, v2, v1
	v_mul_f32_e32 v2, 0x3fb8aa3b, v2
	v_exp_f32_e32 v2, v2
	ds_write_b32 v53, v2 offset:53248
	s_and_saveexec_b64 s[58:59], s[42:43]
	s_cbranch_execz .LBB0_624
	s_lshl_b32 s4, s96, 1
	s_and_b32 s21, s94, -8
	s_or_b32 s62, s4, s21
	s_ashr_i32 s63, s62, 31
	s_lshl_b64 s[62:63], s[62:63], 2
	s_add_u32 s62, s90, s62
	s_addc_u32 s63, s91, s63
	global_store_dwordx2 v137, v[0:1], s[62:63] nt

.LBB0_636:
	v_mul_f32_e32 v1, 0xbfb8aa3b, v6
	v_exp_f32_e32 v1, v1
	v_lshlrev_b32_e32 v136, 1, v19
	v_add_f32_e32 v1, 1.0, v1
	v_rcp_f32_e32 v10, v1
	v_mul_f32_e32 v1, 0xbfb8aa3b, v7
	v_exp_f32_e32 v1, v1
	s_nop 0
	v_add_f32_e32 v1, 1.0, v1
	v_rcp_f32_e32 v11, v1
	v_mul_f32_e32 v1, 0xbfb8aa3b, v4
	v_exp_f32_e32 v1, v1
	v_pk_mul_f32 v[6:7], v[6:7], v[10:11]
	v_add_f32_e32 v1, 1.0, v1
	v_rcp_f32_e32 v10, v1
	v_mul_f32_e32 v1, 0xbfb8aa3b, v5
	v_exp_f32_e32 v1, v1
	s_nop 0
	v_add_f32_e32 v1, 1.0, v1
	v_rcp_f32_e32 v11, v1
	v_mul_f32_e32 v1, 0xbfb8aa3b, v2
	v_exp_f32_e32 v1, v1
	v_pk_mul_f32 v[4:5], v[4:5], v[10:11]
	v_add_f32_e32 v1, 1.0, v1
	v_rcp_f32_e32 v10, v1
	v_mul_f32_e32 v1, 0xbfb8aa3b, v3
	v_exp_f32_e32 v1, v1
	s_nop 0
	v_add_f32_e32 v1, 1.0, v1
	v_rcp_f32_e32 v11, v1
	v_mul_f32_e32 v1, 0xbfb8aa3b, v8
	v_exp_f32_e32 v1, v1
	v_pk_mul_f32 v[2:3], v[2:3], v[10:11]
	v_add_f32_e32 v1, 1.0, v1
	v_rcp_f32_e32 v10, v1
	v_mul_f32_e32 v1, 0xbfb8aa3b, v9
	v_exp_f32_e32 v1, v1
	s_nop 0
	v_add_f32_e32 v1, 1.0, v1
	v_rcp_f32_e32 v11, v1
	v_ashrrev_i32_e32 v1, 31, v0
	v_pk_mul_f32 v[8:9], v[8:9], v[10:11]
	s_and_saveexec_b64 s[74:75], s[58:59]
	s_xor_b64 s[58:59], exec, s[74:75]
	s_cbranch_execz .LBB0_638
	v_lshlrev_b64 v[0:1], 11, v[0:1]
	v_pk_mul_f32 v[6:7], v[6:7], s[16:17] op_sel_hi:[1,0]
	v_pk_mul_f32 v[10:11], v[4:5], s[16:17] op_sel_hi:[1,0]
	v_pk_mul_f32 v[12:13], v[2:3], s[16:17] op_sel_hi:[1,0]
	v_pk_mul_f32 v[8:9], v[8:9], s[16:17] op_sel_hi:[1,0]
	v_lshl_add_u64 v[0:1], s[68:69], 0, v[0:1]
	v_cvt_pk_bf16_f32 v2, v6, v7
	v_cvt_pk_bf16_f32 v3, v10, v11
	v_cvt_pk_bf16_f32 v4, v12, v13
	v_cvt_pk_bf16_f32 v5, v8, v9
	v_lshl_add_u64 v[0:1], v[0:1], 0, v[136:137]
	global_store_dwordx4 v[0:1], v[2:5], off offset:1024 nt
	s_nop 1
	v_lshl_add_u32 v4, v18, 2, 0
	ds_read_b32 v3, v4 offset:53248
	s_waitcnt lgkmcnt(0)
	v_mul_f32_e32 v0, v6, v3
	v_mul_f32_e32 v1, v7, v3
	v_cvt_pk_bf16_f32 v0, v0, v1
	v_mul_f32_e32 v1, v10, v3
	v_mul_f32_e32 v2, v11, v3
	v_cvt_pk_bf16_f32 v1, v1, v2
	v_mul_f32_e32 v2, v12, v3
	v_mul_f32_e32 v5, v13, v3
	v_cvt_pk_bf16_f32 v2, v2, v5
	v_mul_f32_e32 v5, v8, v3
	v_mul_f32_e32 v3, v9, v3
	v_cvt_pk_bf16_f32 v3, v5, v3
	v_mul_u32_u24_e32 v5, 0x11c, v18
	v_add3_u32 v4, v4, v5, v136
	ds_write_b128 v4, v[0:3]
.LBB0_638:
	s_andn2_saveexec_b64 s[58:59], s[58:59]
	s_cbranch_execz .LBB0_627
	v_lshlrev_b64 v[0:1], 11, v[0:1]
	v_lshl_add_u64 v[0:1], s[68:69], 0, v[0:1]
	v_cvt_pk_bf16_f32 v10, v6, v7
	v_cvt_pk_bf16_f32 v11, v4, v5
	v_cvt_pk_bf16_f32 v12, v2, v3
	v_cvt_pk_bf16_f32 v13, v8, v9
	v_lshl_add_u64 v[0:1], v[0:1], 0, v[136:137]
	global_store_dwordx4 v[0:1], v[10:13], off nt
	s_branch .LBB0_627

.LBB0_646:
	s_or_b64 exec, exec, s[58:59]
	s_waitcnt lgkmcnt(0)
	s_barrier
	ds_read_b64_tr_b16 v[28:29], v59
	ds_read_b64_tr_b16 v[30:31], v59 offset:1152
	ds_read_b64_tr_b16 v[0:1], v60 offset:18432
	ds_read_b64_tr_b16 v[2:3], v60 offset:20608
	ds_read_b64_tr_b16 v[20:21], v59 offset:4608
	ds_read_b64_tr_b16 v[22:23], v59 offset:5760
	ds_read_b64_tr_b16 v[16:17], v60 offset:27136
	ds_read_b64_tr_b16 v[18:19], v60 offset:29312
	s_waitcnt lgkmcnt(4)
	v_mfma_f32_32x32x16_bf16 v[0:15], v[28:31], v[0:3], 0
	s_and_b32 s4, s94, -8
	s_or_b32 s58, s96, s4
	s_ashr_i32 s59, s58, 31
	s_lshl_b64 s[58:59], s[58:59], 16
	v_lshl_add_u64 v[48:49], v[34:35], 0, s[58:59]
	s_and_b64 s[58:59], s[6:7], s[38:39]
	s_waitcnt lgkmcnt(0)
	v_mfma_f32_32x32x16_bf16 v[0:15], v[20:23], v[16:19], v[0:15]
	ds_read_b64_tr_b16 v[24:25], v59 offset:9216
	ds_read_b64_tr_b16 v[26:27], v59 offset:10368
	ds_read_b64_tr_b16 v[16:17], v60 offset:35840
	ds_read_b64_tr_b16 v[18:19], v60 offset:38016
	s_waitcnt lgkmcnt(0)
	v_mfma_f32_32x32x16_bf16 v[0:15], v[24:27], v[16:19], v[0:15]
	ds_read_b64_tr_b16 v[16:17], v59 offset:13824
	ds_read_b64_tr_b16 v[18:19], v59 offset:14976
	ds_read_b64_tr_b16 v[64:65], v60 offset:44544
	ds_read_b64_tr_b16 v[66:67], v60 offset:46720
	s_waitcnt lgkmcnt(0)
	v_mfma_f32_32x32x16_bf16 v[0:15], v[16:19], v[64:67], v[0:15]
	s_nop 11
	v_cvt_pk_bf16_f32 v0, v0, v1
	v_cvt_pk_bf16_f32 v1, v2, v3
	v_lshl_add_u64 v[2:3], v[36:37], 1, v[48:49]
	global_store_dwordx2 v[2:3], v[0:1], off nt
	v_cvt_pk_bf16_f32 v0, v4, v5
	v_cvt_pk_bf16_f32 v1, v6, v7
	global_store_dwordx2 v[2:3], v[0:1], off offset:512 nt
	v_cvt_pk_bf16_f32 v0, v8, v9
	v_cvt_pk_bf16_f32 v1, v10, v11
	global_store_dwordx2 v[2:3], v[0:1], off offset:1024 nt
	v_cvt_pk_bf16_f32 v0, v12, v13
	v_cvt_pk_bf16_f32 v1, v14, v15
	global_store_dwordx2 v[2:3], v[0:1], off offset:1536 nt
	ds_read_b64_tr_b16 v[0:1], v61 offset:18432
	ds_read_b64_tr_b16 v[2:3], v61 offset:20608
	s_waitcnt lgkmcnt(0)
	v_mfma_f32_32x32x16_bf16 v[0:15], v[28:31], v[0:3], 0
	ds_read_b64_tr_b16 v[64:65], v61 offset:27136
	ds_read_b64_tr_b16 v[66:67], v61 offset:29312
	s_waitcnt lgkmcnt(0)
	v_mfma_f32_32x32x16_bf16 v[0:15], v[20:23], v[64:67], v[0:15]
	ds_read_b64_tr_b16 v[64:65], v61 offset:35840
	ds_read_b64_tr_b16 v[66:67], v61 offset:38016
	s_waitcnt lgkmcnt(0)
	v_mfma_f32_32x32x16_bf16 v[0:15], v[24:27], v[64:67], v[0:15]
	ds_read_b64_tr_b16 v[64:65], v61 offset:44544
	ds_read_b64_tr_b16 v[66:67], v61 offset:46720
	s_waitcnt lgkmcnt(0)
	v_mfma_f32_32x32x16_bf16 v[0:15], v[16:19], v[64:67], v[0:15]
	s_nop 11
	v_cvt_pk_bf16_f32 v0, v0, v1
	v_cvt_pk_bf16_f32 v1, v2, v3
	v_lshl_add_u64 v[2:3], v[38:39], 1, v[48:49]
	global_store_dwordx2 v[2:3], v[0:1], off nt
	v_cvt_pk_bf16_f32 v0, v4, v5
	v_cvt_pk_bf16_f32 v1, v6, v7
	global_store_dwordx2 v[2:3], v[0:1], off offset:512 nt
	v_cvt_pk_bf16_f32 v0, v8, v9
	v_cvt_pk_bf16_f32 v1, v10, v11
	global_store_dwordx2 v[2:3], v[0:1], off offset:1024 nt
	v_cvt_pk_bf16_f32 v0, v12, v13
	v_cvt_pk_bf16_f32 v1, v14, v15
	global_store_dwordx2 v[2:3], v[0:1], off offset:1536 nt
	ds_read_b64_tr_b16 v[0:1], v62 offset:18432
	ds_read_b64_tr_b16 v[2:3], v62 offset:20608
	s_waitcnt lgkmcnt(0)
	v_mfma_f32_32x32x16_bf16 v[0:15], v[28:31], v[0:3], 0
	ds_read_b64_tr_b16 v[64:65], v62 offset:27136
	ds_read_b64_tr_b16 v[66:67], v62 offset:29312
	s_waitcnt lgkmcnt(0)
	v_mfma_f32_32x32x16_bf16 v[0:15], v[20:23], v[64:67], v[0:15]
	ds_read_b64_tr_b16 v[64:65], v62 offset:35840
	ds_read_b64_tr_b16 v[66:67], v62 offset:38016
	s_waitcnt lgkmcnt(0)
	v_mfma_f32_32x32x16_bf16 v[0:15], v[24:27], v[64:67], v[0:15]
	ds_read_b64_tr_b16 v[64:65], v62 offset:44544
	ds_read_b64_tr_b16 v[66:67], v62 offset:46720
	s_waitcnt lgkmcnt(0)
	v_mfma_f32_32x32x16_bf16 v[0:15], v[16:19], v[64:67], v[0:15]
	s_nop 11
	v_cvt_pk_bf16_f32 v0, v0, v1
	v_cvt_pk_bf16_f32 v1, v2, v3
	v_lshl_add_u64 v[2:3], v[40:41], 1, v[48:49]
	global_store_dwordx2 v[2:3], v[0:1], off nt
	v_cvt_pk_bf16_f32 v0, v4, v5
	v_cvt_pk_bf16_f32 v1, v6, v7
	global_store_dwordx2 v[2:3], v[0:1], off offset:512 nt
	v_cvt_pk_bf16_f32 v0, v8, v9
	v_cvt_pk_bf16_f32 v1, v10, v11
	global_store_dwordx2 v[2:3], v[0:1], off offset:1024 nt
	v_cvt_pk_bf16_f32 v0, v12, v13
	v_cvt_pk_bf16_f32 v1, v14, v15
	global_store_dwordx2 v[2:3], v[0:1], off offset:1536 nt
	ds_read_b64_tr_b16 v[0:1], v63 offset:18432
	ds_read_b64_tr_b16 v[2:3], v63 offset:20608
	s_waitcnt lgkmcnt(0)
	v_mfma_f32_32x32x16_bf16 v[0:15], v[28:31], v[0:3], 0
	ds_read_b64_tr_b16 v[28:29], v63 offset:27136
	ds_read_b64_tr_b16 v[30:31], v63 offset:29312
	s_waitcnt lgkmcnt(0)
	v_mfma_f32_32x32x16_bf16 v[0:15], v[20:23], v[28:31], v[0:15]
	ds_read_b64_tr_b16 v[20:21], v63 offset:35840
	ds_read_b64_tr_b16 v[22:23], v63 offset:38016
	s_waitcnt lgkmcnt(0)
	v_mfma_f32_32x32x16_bf16 v[0:15], v[24:27], v[20:23], v[0:15]
	ds_read_b64_tr_b16 v[20:21], v63 offset:44544
	ds_read_b64_tr_b16 v[22:23], v63 offset:46720
	s_waitcnt lgkmcnt(0)
	v_mfma_f32_32x32x16_bf16 v[0:15], v[16:19], v[20:23], v[0:15]
	s_nop 11
	v_cvt_pk_bf16_f32 v0, v0, v1
	v_cvt_pk_bf16_f32 v1, v2, v3
	v_lshl_add_u64 v[2:3], v[42:43], 1, v[48:49]
	global_store_dwordx2 v[2:3], v[0:1], off nt
	v_cvt_pk_bf16_f32 v0, v4, v5
	v_cvt_pk_bf16_f32 v1, v6, v7
	global_store_dwordx2 v[2:3], v[0:1], off offset:512 nt
	v_cvt_pk_bf16_f32 v0, v8, v9
	v_cvt_pk_bf16_f32 v1, v10, v11
	global_store_dwordx2 v[2:3], v[0:1], off offset:1024 nt
	v_cvt_pk_bf16_f32 v0, v12, v13
	v_cvt_pk_bf16_f32 v1, v14, v15
	global_store_dwordx2 v[2:3], v[0:1], off offset:1536 nt
	s_and_saveexec_b64 s[6:7], s[58:59]
	s_movk_i32 s62, 0x120
	s_cbranch_execz .LBB0_608
	v_mov_b32_e32 v0, 0
	s_mov_b32 s4, 0

.LBB0_765:
	v_lshl_add_u64 v[74:75], s[0:1], 0, v[4:5]
	s_mov_b32 s21, 0x3a200000
	v_add_co_u32_e32 v76, vcc, s21, v74
	s_mov_b32 s21, 0x3a280000
	s_nop 0
	v_addc_co_u32_e32 v77, vcc, 0, v75, vcc
	v_add_co_u32_e32 v78, vcc, s21, v74
	s_mov_b32 s21, 0x3a300000
	s_nop 0
	v_addc_co_u32_e32 v79, vcc, 0, v75, vcc
	s_waitcnt vmcnt(32)
	v_add_co_u32_e32 v80, vcc, s21, v74
	s_mov_b32 s21, 0x3a380000
	s_nop 0
	v_addc_co_u32_e32 v81, vcc, 0, v75, vcc
	v_add_co_u32_e32 v82, vcc, s21, v74
	s_mov_b32 s21, 0x3a400000
	s_nop 0
	v_addc_co_u32_e32 v83, vcc, 0, v75, vcc
	v_add_co_u32_e32 v84, vcc, s21, v74
	s_mov_b32 s21, 0x3a480000
	s_nop 0
	v_addc_co_u32_e32 v85, vcc, 0, v75, vcc
	v_add_co_u32_e32 v86, vcc, s21, v74
	s_mov_b32 s21, 0x3a500000
	s_nop 0
	v_addc_co_u32_e32 v87, vcc, 0, v75, vcc
	v_add_co_u32_e32 v88, vcc, s21, v74
	s_mov_b32 s21, 0x3a580000
	s_nop 0
	v_addc_co_u32_e32 v89, vcc, 0, v75, vcc
	v_add_co_u32_e32 v90, vcc, s21, v74
	s_mov_b32 s21, 0x3a600000
	s_nop 0
	v_addc_co_u32_e32 v91, vcc, 0, v75, vcc
	global_load_dword v205, v[76:77], off
	global_load_dword v204, v[78:79], off
	global_load_dword v203, v[80:81], off
	global_load_dword v202, v[82:83], off
	global_load_dword v185, v[84:85], off
	global_load_dword v184, v[86:87], off
	global_load_dword v183, v[88:89], off
	global_load_dword v182, v[90:91], off
	v_add_co_u32_e32 v76, vcc, s21, v74
	s_mov_b32 s21, 0x3a680000
	s_nop 0
	v_addc_co_u32_e32 v77, vcc, 0, v75, vcc
	v_add_co_u32_e32 v78, vcc, s21, v74
	s_mov_b32 s21, 0x3a700000
	s_nop 0
	v_addc_co_u32_e32 v79, vcc, 0, v75, vcc
	v_add_co_u32_e32 v80, vcc, s21, v74
	s_mov_b32 s21, 0x3a780000
	s_nop 0
	v_addc_co_u32_e32 v81, vcc, 0, v75, vcc
	v_add_co_u32_e32 v82, vcc, s21, v74
	s_mov_b32 s21, 0x3a800000
	s_nop 0
	v_addc_co_u32_e32 v83, vcc, 0, v75, vcc
	v_add_co_u32_e32 v84, vcc, s21, v74
	s_mov_b32 s21, 0x3a880000
	s_nop 0
	v_addc_co_u32_e32 v85, vcc, 0, v75, vcc
	v_add_co_u32_e32 v86, vcc, s21, v74
	s_mov_b32 s21, 0x3a900000
	s_nop 0
	v_addc_co_u32_e32 v87, vcc, 0, v75, vcc
	v_add_co_u32_e32 v88, vcc, s21, v74
	s_mov_b32 s21, 0x3a980000
	s_nop 0
	v_addc_co_u32_e32 v89, vcc, 0, v75, vcc
	v_add_co_u32_e32 v90, vcc, s21, v74
	s_mov_b32 s21, 0x24600000
	s_nop 0
	v_addc_co_u32_e32 v91, vcc, 0, v75, vcc
	global_load_dword v181, v[76:77], off
	global_load_dword v180, v[78:79], off
	global_load_dword v179, v[80:81], off
	global_load_dword v178, v[82:83], off
	global_load_dword v177, v[84:85], off
	global_load_dword v176, v[86:87], off
	global_load_dword v175, v[88:89], off
	global_load_dword v174, v[90:91], off
	v_lshl_add_u64 v[76:77], s[0:1], 0, v[0:1]
	v_add_co_u32_e32 v148, vcc, s21, v76
	s_mov_b32 s21, 0x24708000
	s_nop 0
	v_addc_co_u32_e32 v149, vcc, 0, v77, vcc
	v_lshl_add_u64 v[76:77], s[0:1], 0, v[2:3]
	v_add_co_u32_e32 v80, vcc, s21, v76
	s_mov_b32 s21, 0x24709000
	s_nop 0
	v_addc_co_u32_e32 v81, vcc, 0, v77, vcc
	v_add_co_u32_e32 v84, vcc, s21, v76
	s_mov_b32 s21, 0x2470a000
	s_nop 0
	v_addc_co_u32_e32 v85, vcc, 0, v77, vcc
	v_add_co_u32_e32 v88, vcc, s21, v76
	s_mov_b32 s21, 0x2470b000
	s_nop 0
	v_addc_co_u32_e32 v89, vcc, 0, v77, vcc
	v_add_co_u32_e32 v92, vcc, s21, v76
	global_load_dwordx2 v[144:145], v[148:149], off offset:512
	global_load_dwordx2 v[134:135], v[148:149], off offset:544
	global_load_dwordx2 v[130:131], v[148:149], off offset:576
	global_load_dwordx2 v[126:127], v[148:149], off offset:608
	global_load_dwordx2 v[122:123], v[148:149], off offset:640
	global_load_dwordx2 v[118:119], v[148:149], off offset:672
	global_load_dwordx2 v[114:115], v[148:149], off offset:704
	global_load_dwordx2 v[110:111], v[148:149], off offset:736
	global_load_dwordx2 v[106:107], v[148:149], off offset:768
	global_load_dwordx2 v[102:103], v[148:149], off offset:800
	global_load_dwordx2 v[98:99], v[148:149], off offset:832
	global_load_dwordx2 v[94:95], v[148:149], off offset:864
	global_load_dwordx2 v[90:91], v[148:149], off offset:896
	global_load_dwordx2 v[86:87], v[148:149], off offset:928
	global_load_dwordx2 v[82:83], v[148:149], off offset:960
	global_load_dwordx2 v[78:79], v[148:149], off offset:992
	v_addc_co_u32_e32 v93, vcc, 0, v77, vcc
	s_mov_b32 s21, 0x2470c000
	global_load_dwordx2 v[146:147], v[84:85], off offset:-4096
	global_load_dwordx2 v[132:133], v[84:85], off
	global_load_dwordx2 v[128:129], v[84:85], off offset:2048
	global_load_dwordx2 v[124:125], v[92:93], off offset:-4096
	v_add_co_u32_e32 v84, vcc, s21, v76
	s_mov_b32 s21, 0x2470d000
	s_nop 0
	v_addc_co_u32_e32 v85, vcc, 0, v77, vcc
	v_add_co_u32_e32 v96, vcc, s21, v76
	s_mov_b32 s21, 0x2470e000
	s_nop 0
	v_addc_co_u32_e32 v97, vcc, 0, v77, vcc
	global_load_dwordx2 v[116:117], v[92:93], off
	global_load_dwordx2 v[112:113], v[92:93], off offset:2048
	global_load_dwordx2 v[108:109], v[96:97], off offset:-4096
	global_load_dwordx2 v[100:101], v[96:97], off
	v_add_co_u32_e32 v92, vcc, s21, v76
	s_mov_b32 s21, 0x2470f000
	s_nop 0
	v_addc_co_u32_e32 v93, vcc, 0, v77, vcc
	v_add_co_u32_e32 v152, vcc, s21, v76
	s_nop 1
	v_addc_co_u32_e32 v153, vcc, 0, v77, vcc
	global_load_dwordx2 v[142:143], v[80:81], off offset:2048
	global_load_dwordx2 v[120:121], v[88:89], off offset:2048
	global_load_dwordx2 v[104:105], v[84:85], off offset:2048
	s_nop 0
	global_load_dwordx2 v[88:89], v[92:93], off offset:2048
	s_nop 0
	global_load_dwordx2 v[96:97], v[96:97], off offset:2048
	s_nop 0
	global_load_dwordx2 v[92:93], v[152:153], off offset:-4096
	global_load_dwordx2 v[84:85], v[152:153], off
	global_load_dwordx2 v[80:81], v[152:153], off offset:2048
	s_waitcnt vmcnt(62)
	v_add_f32_e32 v136, v8, v207
	v_max_f32_e32 v138, v9, v9
	v_max_f32_e32 v208, v136, v138
	v_sub_f32_e32 v136, v136, v208
	v_mul_f32_e32 v136, 0x3fb8aa3b, v136
	v_exp_f32_e32 v152, v136
	v_sub_f32_e32 v136, v9, v208
	v_mul_f32_e32 v136, 0x3fb8aa3b, v136
	v_exp_f32_e32 v154, v136
	v_add_co_u32_e32 v210, vcc, 0x39a00000, v74
	v_cvt_pk_bf16_f32 v136, v150, v151
	s_nop 0
	v_addc_co_u32_e32 v211, vcc, 0, v75, vcc
	v_mov_b32_e32 v153, v152
	v_mov_b32_e32 v155, v154
	global_store_dword v[210:211], v136, off
	s_and_saveexec_b64 s[44:45], s[38:39]
	s_cbranch_execz .LBB0_769
	v_add_co_u32_e32 v210, vcc, 0x24700000, v76
	s_nop 1
	v_addc_co_u32_e32 v211, vcc, 0, v77, vcc
	global_store_dwordx2 v[210:211], v[40:41], off nt
	s_and_saveexec_b64 s[46:47], s[40:41]
	s_cbranch_execz .LBB0_768
	v_lshl_add_u64 v[210:211], s[0:1], 0, v[6:7]
	v_add_co_u32_e32 v210, vcc, 0x24610000, v210
	s_nop 1
	v_addc_co_u32_e32 v211, vcc, 0, v211, vcc
	global_store_dword v[210:211], v207, off

.LBB0_769:
	s_or_b64 exec, exec, s[44:45]
	s_waitcnt vmcnt(56)
	v_lshlrev_b32_e32 v206, 16, v167
	v_and_b32_e32 v207, 0xffff0000, v167
	v_add_f32_e32 v136, v10, v208
	v_max_f32_e32 v138, v11, v11
	v_pk_mul_f32 v[154:155], v[154:155], v[206:207]
	v_max_f32_e32 v206, v136, v138
	v_sub_f32_e32 v136, v136, v206
	v_sub_f32_e32 v138, v11, v206
	v_mul_f32_e32 v136, 0x3fb8aa3b, v136
	v_mul_f32_e32 v138, 0x3fb8aa3b, v138
	v_pk_fma_f32 v[150:151], v[150:151], v[152:153], v[154:155]
	v_exp_f32_e32 v136, v136
	v_exp_f32_e32 v152, v138
	v_add_co_u32_e32 v154, vcc, 0x39a80000, v74
	v_cvt_pk_bf16_f32 v138, v150, v151
	s_nop 0
	v_addc_co_u32_e32 v155, vcc, 0, v75, vcc
	global_store_dword v[154:155], v138, off
	s_and_saveexec_b64 s[44:45], s[38:39]
	s_cbranch_execz .LBB0_773
	v_add_co_u32_e32 v154, vcc, 0x24700000, v76
	s_nop 1
	v_addc_co_u32_e32 v155, vcc, 0, v77, vcc
	global_store_dwordx2 v[154:155], v[40:41], off offset:2048 nt
	s_and_saveexec_b64 s[46:47], s[40:41]
	s_cbranch_execz .LBB0_772
	v_lshl_add_u64 v[154:155], s[0:1], 0, v[6:7]
	v_add_co_u32_e32 v154, vcc, 0x24610000, v154
	s_nop 1
	v_addc_co_u32_e32 v155, vcc, 0, v155, vcc
	global_store_dword v[154:155], v208, off offset:16

.LBB0_773:
	s_or_b64 exec, exec, s[44:45]
	v_lshlrev_b32_e32 v154, 16, v159
	v_and_b32_e32 v155, 0xffff0000, v159
	v_pk_mul_f32 v[152:153], v[152:153], v[154:155] op_sel_hi:[0,1]
	v_pk_fma_f32 v[150:151], v[150:151], v[136:137], v[152:153] op_sel_hi:[1,0,1]
	v_add_f32_e32 v138, v12, v206
	v_max_f32_e32 v136, v13, v13
	v_max_f32_e32 v136, v138, v136
	v_sub_f32_e32 v138, v138, v136
	v_mul_f32_e32 v138, 0x3fb8aa3b, v138
	v_exp_f32_e32 v152, v138
	v_sub_f32_e32 v138, v13, v136
	v_mul_f32_e32 v138, 0x3fb8aa3b, v138
	v_exp_f32_e32 v154, v138
	v_add_co_u32_e32 v208, vcc, 0x39b00000, v74
	v_cvt_pk_bf16_f32 v138, v150, v151
	s_nop 0
	v_addc_co_u32_e32 v209, vcc, 0, v75, vcc
	v_mov_b32_e32 v153, v152
	v_mov_b32_e32 v155, v154
	global_store_dword v[208:209], v138, off
	s_and_saveexec_b64 s[44:45], s[38:39]
	s_cbranch_execz .LBB0_777
	v_add_co_u32_e32 v208, vcc, 0x24701000, v76
	s_nop 1
	v_addc_co_u32_e32 v209, vcc, 0, v77, vcc
	global_store_dwordx2 v[208:209], v[40:41], off nt
	s_and_saveexec_b64 s[46:47], s[40:41]
	s_cbranch_execz .LBB0_776
	v_lshl_add_u64 v[208:209], s[0:1], 0, v[6:7]
	v_add_co_u32_e32 v208, vcc, 0x24610000, v208
	s_nop 1
	v_addc_co_u32_e32 v209, vcc, 0, v209, vcc
	global_store_dword v[208:209], v206, off offset:32

.LBB0_777:
	s_or_b64 exec, exec, s[44:45]
	v_lshlrev_b32_e32 v206, 16, v160
	v_and_b32_e32 v207, 0xffff0000, v160
	v_add_f32_e32 v138, v14, v136
	v_max_f32_e32 v139, v15, v15
	v_pk_mul_f32 v[154:155], v[154:155], v[206:207]
	v_max_f32_e32 v206, v138, v139
	v_sub_f32_e32 v138, v138, v206
	v_mul_f32_e32 v138, 0x3fb8aa3b, v138
	v_pk_fma_f32 v[150:151], v[150:151], v[152:153], v[154:155]
	v_exp_f32_e32 v152, v138
	v_sub_f32_e32 v138, v15, v206
	v_mul_f32_e32 v138, 0x3fb8aa3b, v138
	v_exp_f32_e32 v154, v138
	v_add_co_u32_e32 v208, vcc, 0x39b80000, v74
	v_cvt_pk_bf16_f32 v138, v150, v151
	s_nop 0
	v_addc_co_u32_e32 v209, vcc, 0, v75, vcc
	v_mov_b32_e32 v153, v152
	v_mov_b32_e32 v155, v154
	global_store_dword v[208:209], v138, off
	s_and_saveexec_b64 s[44:45], s[38:39]
	s_cbranch_execz .LBB0_781
	v_add_co_u32_e32 v208, vcc, 0x24701000, v76
	s_nop 1
	v_addc_co_u32_e32 v209, vcc, 0, v77, vcc
	global_store_dwordx2 v[208:209], v[40:41], off offset:2048 nt
	s_and_saveexec_b64 s[46:47], s[40:41]
	s_cbranch_execz .LBB0_780
	v_lshl_add_u64 v[208:209], s[0:1], 0, v[6:7]
	v_add_co_u32_e32 v208, vcc, 0x24610000, v208
	s_nop 1
	v_addc_co_u32_e32 v209, vcc, 0, v209, vcc
	global_store_dword v[208:209], v136, off offset:48

.LBB0_781:
	s_or_b64 exec, exec, s[44:45]
	v_add_f32_e32 v138, v16, v206
	v_max_f32_e32 v136, v17, v17
	v_max_f32_e32 v136, v138, v136
	v_lshlrev_b32_e32 v208, 16, v161
	v_and_b32_e32 v209, 0xffff0000, v161
	v_sub_f32_e32 v138, v138, v136
	v_pk_mul_f32 v[154:155], v[154:155], v[208:209]
	v_mul_f32_e32 v138, 0x3fb8aa3b, v138
	v_pk_fma_f32 v[150:151], v[150:151], v[152:153], v[154:155]
	v_exp_f32_e32 v152, v138
	v_sub_f32_e32 v138, v17, v136
	v_mul_f32_e32 v138, 0x3fb8aa3b, v138
	v_exp_f32_e32 v154, v138
	v_add_co_u32_e32 v208, vcc, 0x39c00000, v74
	v_cvt_pk_bf16_f32 v138, v150, v151
	s_nop 0
	v_addc_co_u32_e32 v209, vcc, 0, v75, vcc
	v_mov_b32_e32 v153, v152
	v_mov_b32_e32 v155, v154
	global_store_dword v[208:209], v138, off
	s_and_saveexec_b64 s[44:45], s[38:39]
	s_cbranch_execz .LBB0_785
	v_add_co_u32_e32 v208, vcc, 0x24702000, v76
	s_nop 1
	v_addc_co_u32_e32 v209, vcc, 0, v77, vcc
	global_store_dwordx2 v[208:209], v[40:41], off nt
	s_and_saveexec_b64 s[46:47], s[40:41]
	s_cbranch_execz .LBB0_784
	v_lshl_add_u64 v[208:209], s[0:1], 0, v[6:7]
	v_add_co_u32_e32 v208, vcc, 0x24610000, v208
	s_nop 1
	v_addc_co_u32_e32 v209, vcc, 0, v209, vcc
	global_store_dword v[208:209], v206, off offset:64

.LBB0_785:
	s_or_b64 exec, exec, s[44:45]
	v_lshlrev_b32_e32 v206, 16, v162
	v_and_b32_e32 v207, 0xffff0000, v162
	v_add_f32_e32 v138, v18, v136
	v_max_f32_e32 v139, v19, v19
	v_pk_mul_f32 v[154:155], v[154:155], v[206:207]
	v_max_f32_e32 v207, v138, v139
	v_sub_f32_e32 v138, v138, v207
	v_mul_f32_e32 v138, 0x3fb8aa3b, v138
	v_pk_fma_f32 v[150:151], v[150:151], v[152:153], v[154:155]
	v_exp_f32_e32 v152, v138
	v_sub_f32_e32 v138, v19, v207
	v_mul_f32_e32 v138, 0x3fb8aa3b, v138
	v_exp_f32_e32 v154, v138
	v_add_co_u32_e32 v208, vcc, 0x39c80000, v74
	v_cvt_pk_bf16_f32 v138, v150, v151
	s_nop 0
	v_addc_co_u32_e32 v209, vcc, 0, v75, vcc
	v_mov_b32_e32 v153, v152
	v_mov_b32_e32 v155, v154
	global_store_dword v[208:209], v138, off
	s_and_saveexec_b64 s[44:45], s[38:39]
	s_cbranch_execz .LBB0_789
	v_add_co_u32_e32 v208, vcc, 0x24702000, v76
	s_nop 1
	v_addc_co_u32_e32 v209, vcc, 0, v77, vcc
	global_store_dwordx2 v[208:209], v[40:41], off offset:2048 nt
	s_and_saveexec_b64 s[46:47], s[40:41]
	s_cbranch_execz .LBB0_788
	v_lshl_add_u64 v[208:209], s[0:1], 0, v[6:7]
	v_add_co_u32_e32 v208, vcc, 0x24610000, v208
	s_nop 1
	v_addc_co_u32_e32 v209, vcc, 0, v209, vcc
	global_store_dword v[208:209], v136, off offset:80

.LBB0_789:
	s_or_b64 exec, exec, s[44:45]
	v_add_f32_e32 v136, v20, v207
	v_max_f32_e32 v138, v21, v21
	v_max_f32_e32 v206, v136, v138
	v_lshlrev_b32_e32 v208, 16, v163
	v_and_b32_e32 v209, 0xffff0000, v163
	v_sub_f32_e32 v136, v136, v206
	v_sub_f32_e32 v138, v21, v206
	v_pk_mul_f32 v[154:155], v[154:155], v[208:209]
	v_mul_f32_e32 v136, 0x3fb8aa3b, v136
	v_mul_f32_e32 v138, 0x3fb8aa3b, v138
	v_pk_fma_f32 v[150:151], v[150:151], v[152:153], v[154:155]
	v_exp_f32_e32 v136, v136
	v_exp_f32_e32 v152, v138
	v_add_co_u32_e32 v154, vcc, 0x39d00000, v74
	v_cvt_pk_bf16_f32 v138, v150, v151
	s_nop 0
	v_addc_co_u32_e32 v155, vcc, 0, v75, vcc
	global_store_dword v[154:155], v138, off
	s_and_saveexec_b64 s[44:45], s[38:39]
	s_cbranch_execz .LBB0_793
	v_add_co_u32_e32 v154, vcc, 0x24703000, v76
	s_nop 1
	v_addc_co_u32_e32 v155, vcc, 0, v77, vcc
	global_store_dwordx2 v[154:155], v[40:41], off nt
	s_and_saveexec_b64 s[46:47], s[40:41]
	s_cbranch_execz .LBB0_792
	v_lshl_add_u64 v[154:155], s[0:1], 0, v[6:7]
	v_add_co_u32_e32 v154, vcc, 0x24610000, v154
	s_nop 1
	v_addc_co_u32_e32 v155, vcc, 0, v155, vcc
	global_store_dword v[154:155], v207, off offset:96

.LBB0_793:
	s_or_b64 exec, exec, s[44:45]
	v_lshlrev_b32_e32 v154, 16, v164
	v_and_b32_e32 v155, 0xffff0000, v164
	v_pk_mul_f32 v[152:153], v[152:153], v[154:155] op_sel_hi:[0,1]
	v_pk_fma_f32 v[150:151], v[150:151], v[136:137], v[152:153] op_sel_hi:[1,0,1]
	v_add_f32_e32 v138, v22, v206
	v_max_f32_e32 v136, v23, v23
	v_max_f32_e32 v136, v138, v136
	v_sub_f32_e32 v138, v138, v136
	v_mul_f32_e32 v138, 0x3fb8aa3b, v138
	v_exp_f32_e32 v152, v138
	v_sub_f32_e32 v138, v23, v136
	v_mul_f32_e32 v138, 0x3fb8aa3b, v138
	v_exp_f32_e32 v154, v138
	v_add_co_u32_e32 v208, vcc, 0x39d80000, v74
	v_cvt_pk_bf16_f32 v138, v150, v151
	s_nop 0
	v_addc_co_u32_e32 v209, vcc, 0, v75, vcc
	v_mov_b32_e32 v153, v152
	v_mov_b32_e32 v155, v154
	global_store_dword v[208:209], v138, off
	s_and_saveexec_b64 s[44:45], s[38:39]
	s_cbranch_execz .LBB0_797
	v_add_co_u32_e32 v208, vcc, 0x24703000, v76
	s_nop 1
	v_addc_co_u32_e32 v209, vcc, 0, v77, vcc
	global_store_dwordx2 v[208:209], v[40:41], off offset:2048 nt
	s_and_saveexec_b64 s[46:47], s[40:41]
	s_cbranch_execz .LBB0_796
	v_lshl_add_u64 v[208:209], s[0:1], 0, v[6:7]
	v_add_co_u32_e32 v208, vcc, 0x24610000, v208
	s_nop 1
	v_addc_co_u32_e32 v209, vcc, 0, v209, vcc
	global_store_dword v[208:209], v206, off offset:112

.LBB0_797:
	s_or_b64 exec, exec, s[44:45]
	v_lshlrev_b32_e32 v206, 16, v165
	v_and_b32_e32 v207, 0xffff0000, v165
	v_add_f32_e32 v138, v24, v136
	v_max_f32_e32 v139, v25, v25
	v_pk_mul_f32 v[154:155], v[154:155], v[206:207]
	v_max_f32_e32 v206, v138, v139
	v_sub_f32_e32 v138, v138, v206
	v_mul_f32_e32 v138, 0x3fb8aa3b, v138
	v_pk_fma_f32 v[150:151], v[150:151], v[152:153], v[154:155]
	v_exp_f32_e32 v152, v138
	v_sub_f32_e32 v138, v25, v206
	v_mul_f32_e32 v138, 0x3fb8aa3b, v138
	v_exp_f32_e32 v154, v138
	v_add_co_u32_e32 v208, vcc, 0x39e00000, v74
	v_cvt_pk_bf16_f32 v138, v150, v151
	s_nop 0
	v_addc_co_u32_e32 v209, vcc, 0, v75, vcc
	v_mov_b32_e32 v153, v152
	v_mov_b32_e32 v155, v154
	global_store_dword v[208:209], v138, off
	s_and_saveexec_b64 s[44:45], s[38:39]
	s_cbranch_execz .LBB0_801
	v_add_co_u32_e32 v208, vcc, 0x24704000, v76
	s_nop 1
	v_addc_co_u32_e32 v209, vcc, 0, v77, vcc
	global_store_dwordx2 v[208:209], v[40:41], off nt
	s_and_saveexec_b64 s[46:47], s[40:41]
	s_cbranch_execz .LBB0_800
	v_lshl_add_u64 v[208:209], s[0:1], 0, v[6:7]
	v_add_co_u32_e32 v208, vcc, 0x24610000, v208
	s_nop 1
	v_addc_co_u32_e32 v209, vcc, 0, v209, vcc
	global_store_dword v[208:209], v136, off offset:128

.LBB0_801:
	s_or_b64 exec, exec, s[44:45]
	v_add_f32_e32 v138, v26, v206
	v_max_f32_e32 v136, v27, v27
	v_max_f32_e32 v136, v138, v136
	v_lshlrev_b32_e32 v208, 16, v166
	v_and_b32_e32 v209, 0xffff0000, v166
	v_sub_f32_e32 v138, v138, v136
	v_pk_mul_f32 v[154:155], v[154:155], v[208:209]
	v_mul_f32_e32 v138, 0x3fb8aa3b, v138
	v_pk_fma_f32 v[150:151], v[150:151], v[152:153], v[154:155]
	v_exp_f32_e32 v152, v138
	v_sub_f32_e32 v138, v27, v136
	v_mul_f32_e32 v138, 0x3fb8aa3b, v138
	v_exp_f32_e32 v154, v138
	v_add_co_u32_e32 v208, vcc, 0x39e80000, v74
	v_cvt_pk_bf16_f32 v138, v150, v151
	s_nop 0
	v_addc_co_u32_e32 v209, vcc, 0, v75, vcc
	v_mov_b32_e32 v153, v152
	v_mov_b32_e32 v155, v154
	global_store_dword v[208:209], v138, off
	s_and_saveexec_b64 s[44:45], s[38:39]
	s_cbranch_execz .LBB0_805
	v_add_co_u32_e32 v208, vcc, 0x24704000, v76
	s_nop 1
	v_addc_co_u32_e32 v209, vcc, 0, v77, vcc
	global_store_dwordx2 v[208:209], v[40:41], off offset:2048 nt
	s_and_saveexec_b64 s[46:47], s[40:41]
	s_cbranch_execz .LBB0_804
	v_lshl_add_u64 v[208:209], s[0:1], 0, v[6:7]
	v_add_co_u32_e32 v208, vcc, 0x24610000, v208
	s_nop 1
	v_addc_co_u32_e32 v209, vcc, 0, v209, vcc
	global_store_dword v[208:209], v206, off offset:144

.LBB0_805:
	s_or_b64 exec, exec, s[44:45]
	v_lshlrev_b32_e32 v206, 16, v168
	v_and_b32_e32 v207, 0xffff0000, v168
	v_add_f32_e32 v138, v28, v136
	v_max_f32_e32 v139, v29, v29
	v_pk_mul_f32 v[154:155], v[154:155], v[206:207]
	v_max_f32_e32 v207, v138, v139
	v_sub_f32_e32 v138, v138, v207
	v_mul_f32_e32 v138, 0x3fb8aa3b, v138
	v_pk_fma_f32 v[150:151], v[150:151], v[152:153], v[154:155]
	v_exp_f32_e32 v152, v138
	v_sub_f32_e32 v138, v29, v207
	v_mul_f32_e32 v138, 0x3fb8aa3b, v138
	v_exp_f32_e32 v154, v138
	v_add_co_u32_e32 v208, vcc, 0x39f00000, v74
	v_cvt_pk_bf16_f32 v138, v150, v151
	s_nop 0
	v_addc_co_u32_e32 v209, vcc, 0, v75, vcc
	v_mov_b32_e32 v153, v152
	v_mov_b32_e32 v155, v154
	global_store_dword v[208:209], v138, off
	s_and_saveexec_b64 s[44:45], s[38:39]
	s_cbranch_execz .LBB0_809
	v_add_co_u32_e32 v208, vcc, 0x24705000, v76
	s_nop 1
	v_addc_co_u32_e32 v209, vcc, 0, v77, vcc
	global_store_dwordx2 v[208:209], v[40:41], off nt
	s_and_saveexec_b64 s[46:47], s[40:41]
	s_cbranch_execz .LBB0_808
	v_lshl_add_u64 v[208:209], s[0:1], 0, v[6:7]
	v_add_co_u32_e32 v208, vcc, 0x24610000, v208
	s_nop 1
	v_addc_co_u32_e32 v209, vcc, 0, v209, vcc
	global_store_dword v[208:209], v136, off offset:160

.LBB0_809:
	s_or_b64 exec, exec, s[44:45]
	v_add_f32_e32 v136, v30, v207
	v_max_f32_e32 v138, v31, v31
	v_max_f32_e32 v206, v136, v138
	v_lshlrev_b32_e32 v208, 16, v169
	v_and_b32_e32 v209, 0xffff0000, v169
	v_sub_f32_e32 v136, v136, v206
	v_sub_f32_e32 v138, v31, v206
	v_pk_mul_f32 v[154:155], v[154:155], v[208:209]
	v_mul_f32_e32 v136, 0x3fb8aa3b, v136
	v_mul_f32_e32 v138, 0x3fb8aa3b, v138
	v_pk_fma_f32 v[150:151], v[150:151], v[152:153], v[154:155]
	v_exp_f32_e32 v136, v136
	v_exp_f32_e32 v152, v138
	v_add_co_u32_e32 v154, vcc, 0x39f80000, v74
	v_cvt_pk_bf16_f32 v138, v150, v151
	s_nop 0
	v_addc_co_u32_e32 v155, vcc, 0, v75, vcc
	global_store_dword v[154:155], v138, off
	s_and_saveexec_b64 s[44:45], s[38:39]
	s_cbranch_execz .LBB0_813
	v_add_co_u32_e32 v154, vcc, 0x24705000, v76
	s_nop 1
	v_addc_co_u32_e32 v155, vcc, 0, v77, vcc
	global_store_dwordx2 v[154:155], v[40:41], off offset:2048 nt
	s_and_saveexec_b64 s[46:47], s[40:41]
	s_cbranch_execz .LBB0_812
	v_lshl_add_u64 v[154:155], s[0:1], 0, v[6:7]
	v_add_co_u32_e32 v154, vcc, 0x24610000, v154
	s_nop 1
	v_addc_co_u32_e32 v155, vcc, 0, v155, vcc
	global_store_dword v[154:155], v207, off offset:176

.LBB0_813:
	s_or_b64 exec, exec, s[44:45]
	v_lshlrev_b32_e32 v154, 16, v170
	v_and_b32_e32 v155, 0xffff0000, v170
	v_pk_mul_f32 v[152:153], v[152:153], v[154:155] op_sel_hi:[0,1]
	v_pk_fma_f32 v[150:151], v[150:151], v[136:137], v[152:153] op_sel_hi:[1,0,1]
	v_add_f32_e32 v138, v32, v206
	v_max_f32_e32 v136, v33, v33
	v_max_f32_e32 v136, v138, v136
	v_sub_f32_e32 v138, v138, v136
	v_mul_f32_e32 v138, 0x3fb8aa3b, v138
	v_exp_f32_e32 v152, v138
	v_sub_f32_e32 v138, v33, v136
	v_mul_f32_e32 v138, 0x3fb8aa3b, v138
	v_exp_f32_e32 v154, v138
	v_add_co_u32_e32 v208, vcc, 0x3a000000, v74
	v_cvt_pk_bf16_f32 v138, v150, v151
	s_nop 0
	v_addc_co_u32_e32 v209, vcc, 0, v75, vcc
	v_mov_b32_e32 v153, v152
	v_mov_b32_e32 v155, v154
	global_store_dword v[208:209], v138, off
	s_and_saveexec_b64 s[44:45], s[38:39]
	s_cbranch_execz .LBB0_817
	v_add_co_u32_e32 v208, vcc, 0x24706000, v76
	s_nop 1
	v_addc_co_u32_e32 v209, vcc, 0, v77, vcc
	global_store_dwordx2 v[208:209], v[40:41], off nt
	s_and_saveexec_b64 s[46:47], s[40:41]
	s_cbranch_execz .LBB0_816
	v_lshl_add_u64 v[208:209], s[0:1], 0, v[6:7]
	v_add_co_u32_e32 v208, vcc, 0x24610000, v208
	s_nop 1
	v_addc_co_u32_e32 v209, vcc, 0, v209, vcc
	global_store_dword v[208:209], v206, off offset:192

.LBB0_817:
	s_or_b64 exec, exec, s[44:45]
	v_lshlrev_b32_e32 v206, 16, v171
	v_and_b32_e32 v207, 0xffff0000, v171
	v_add_f32_e32 v138, v34, v136
	v_max_f32_e32 v139, v35, v35
	v_pk_mul_f32 v[154:155], v[154:155], v[206:207]
	v_max_f32_e32 v206, v138, v139
	v_sub_f32_e32 v138, v138, v206
	v_mul_f32_e32 v138, 0x3fb8aa3b, v138
	v_pk_fma_f32 v[150:151], v[150:151], v[152:153], v[154:155]
	v_exp_f32_e32 v152, v138
	v_sub_f32_e32 v138, v35, v206
	v_mul_f32_e32 v138, 0x3fb8aa3b, v138
	v_exp_f32_e32 v154, v138
	v_add_co_u32_e32 v208, vcc, 0x3a080000, v74
	v_cvt_pk_bf16_f32 v138, v150, v151
	s_nop 0
	v_addc_co_u32_e32 v209, vcc, 0, v75, vcc
	v_mov_b32_e32 v153, v152
	v_mov_b32_e32 v155, v154
	global_store_dword v[208:209], v138, off
	s_and_saveexec_b64 s[44:45], s[38:39]
	s_cbranch_execz .LBB0_821
	v_add_co_u32_e32 v208, vcc, 0x24706000, v76
	s_nop 1
	v_addc_co_u32_e32 v209, vcc, 0, v77, vcc
	global_store_dwordx2 v[208:209], v[40:41], off offset:2048 nt
	s_and_saveexec_b64 s[46:47], s[40:41]
	s_cbranch_execz .LBB0_820
	v_lshl_add_u64 v[208:209], s[0:1], 0, v[6:7]
	v_add_co_u32_e32 v208, vcc, 0x24610000, v208
	s_nop 1
	v_addc_co_u32_e32 v209, vcc, 0, v209, vcc
	global_store_dword v[208:209], v136, off offset:208

.LBB0_821:
	s_or_b64 exec, exec, s[44:45]
	v_add_f32_e32 v138, v36, v206
	v_max_f32_e32 v136, v37, v37
	v_max_f32_e32 v136, v138, v136
	v_lshlrev_b32_e32 v208, 16, v172
	v_and_b32_e32 v209, 0xffff0000, v172
	v_sub_f32_e32 v138, v138, v136
	v_pk_mul_f32 v[154:155], v[154:155], v[208:209]
	v_mul_f32_e32 v138, 0x3fb8aa3b, v138
	v_pk_fma_f32 v[150:151], v[150:151], v[152:153], v[154:155]
	v_exp_f32_e32 v152, v138
	v_sub_f32_e32 v138, v37, v136
	v_mul_f32_e32 v138, 0x3fb8aa3b, v138
	v_exp_f32_e32 v154, v138
	v_add_co_u32_e32 v208, vcc, 0x3a100000, v74
	v_cvt_pk_bf16_f32 v138, v150, v151
	s_nop 0
	v_addc_co_u32_e32 v209, vcc, 0, v75, vcc
	v_mov_b32_e32 v153, v152
	v_mov_b32_e32 v155, v154
	global_store_dword v[208:209], v138, off
	s_and_saveexec_b64 s[44:45], s[38:39]
	s_cbranch_execz .LBB0_825
	v_add_co_u32_e32 v208, vcc, 0x24707000, v76
	s_nop 1
	v_addc_co_u32_e32 v209, vcc, 0, v77, vcc
	global_store_dwordx2 v[208:209], v[40:41], off nt
	s_and_saveexec_b64 s[46:47], s[40:41]
	s_cbranch_execz .LBB0_824
	v_lshl_add_u64 v[208:209], s[0:1], 0, v[6:7]
	v_add_co_u32_e32 v208, vcc, 0x24610000, v208
	s_nop 1
	v_addc_co_u32_e32 v209, vcc, 0, v209, vcc
	global_store_dword v[208:209], v206, off offset:224

.LBB0_825:
	s_or_b64 exec, exec, s[44:45]
	v_lshlrev_b32_e32 v206, 16, v173
	v_and_b32_e32 v207, 0xffff0000, v173
	v_add_f32_e32 v138, v38, v136
	v_max_f32_e32 v139, v39, v39
	v_pk_mul_f32 v[154:155], v[154:155], v[206:207]
	v_max_f32_e32 v207, v138, v139
	v_sub_f32_e32 v138, v138, v207
	v_mul_f32_e32 v138, 0x3fb8aa3b, v138
	v_pk_fma_f32 v[150:151], v[150:151], v[152:153], v[154:155]
	v_exp_f32_e32 v152, v138
	v_sub_f32_e32 v138, v39, v207
	v_mul_f32_e32 v138, 0x3fb8aa3b, v138
	v_exp_f32_e32 v154, v138
	v_add_co_u32_e32 v208, vcc, 0x3a180000, v74
	v_cvt_pk_bf16_f32 v138, v150, v151
	s_nop 0
	v_addc_co_u32_e32 v209, vcc, 0, v75, vcc
	v_mov_b32_e32 v153, v152
	v_mov_b32_e32 v155, v154
	global_store_dword v[208:209], v138, off
	s_and_saveexec_b64 s[44:45], s[38:39]
	s_cbranch_execz .LBB0_829
	v_add_co_u32_e32 v208, vcc, 0x24707000, v76
	s_nop 1
	v_addc_co_u32_e32 v209, vcc, 0, v77, vcc
	global_store_dwordx2 v[208:209], v[40:41], off offset:2048 nt
	s_and_saveexec_b64 s[46:47], s[40:41]
	s_cbranch_execz .LBB0_828
	v_lshl_add_u64 v[208:209], s[0:1], 0, v[6:7]
	v_add_co_u32_e32 v208, vcc, 0x24610000, v208
	s_nop 1
	v_addc_co_u32_e32 v209, vcc, 0, v209, vcc
	global_store_dword v[208:209], v136, off offset:240

.LBB0_831:
	v_lshlrev_b32_e32 v148, 16, v201
	v_and_b32_e32 v149, 0xffff0000, v201
	s_waitcnt vmcnt(47)
	v_add_f32_e32 v136, v144, v207
	v_max_f32_e32 v138, v145, v145
	v_pk_mul_f32 v[210:211], v[154:155], v[148:149]
	v_max_f32_e32 v154, v136, v138
	v_sub_f32_e32 v136, v136, v154
	v_sub_f32_e32 v138, v145, v154
	v_mul_f32_e32 v136, 0x3fb8aa3b, v136
	v_mul_f32_e32 v138, 0x3fb8aa3b, v138
	v_exp_f32_e32 v136, v136
	v_exp_f32_e32 v148, v138
	s_mov_b64 s[46:47], 0x3a200000
	v_pk_fma_f32 v[144:145], v[150:151], v[152:153], v[210:211]
	v_lshl_add_u64 v[208:209], v[74:75], 0, s[46:47]
	v_cvt_pk_bf16_f32 v138, v144, v145
	global_store_dword v[208:209], v138, off
	s_and_saveexec_b64 s[46:47], s[38:39]
	s_cbranch_execz .LBB0_835
	s_mov_b64 s[48:49], 0x24708000
	v_lshl_add_u64 v[150:151], v[76:77], 0, s[48:49]
	global_store_dwordx2 v[150:151], v[40:41], off nt
	s_and_saveexec_b64 s[48:49], s[40:41]
	s_cbranch_execz .LBB0_834
	v_lshl_add_u64 v[150:151], s[0:1], 0, v[6:7]
	v_add_co_u32_e32 v150, vcc, 0x24610000, v150
	s_nop 1
	v_addc_co_u32_e32 v151, vcc, 0, v151, vcc
	global_store_dword v[150:151], v207, off offset:256

.LBB0_835:
	s_or_b64 exec, exec, s[46:47]
	s_waitcnt vmcnt(32)
	v_lshlrev_b32_e32 v146, 16, v205
	v_and_b32_e32 v147, 0xffff0000, v205
	v_pk_mul_f32 v[146:147], v[148:149], v[146:147] op_sel_hi:[0,1]
	v_pk_fma_f32 v[144:145], v[144:145], v[136:137], v[146:147] op_sel_hi:[1,0,1]
	v_add_f32_e32 v134, v134, v154
	v_max_f32_e32 v136, v135, v135
	v_max_f32_e32 v136, v134, v136
	v_sub_f32_e32 v134, v134, v136
	v_sub_f32_e32 v135, v135, v136
	v_mul_f32_e32 v134, 0x3fb8aa3b, v134
	v_mul_f32_e32 v135, 0x3fb8aa3b, v135
	v_exp_f32_e32 v134, v134
	v_exp_f32_e32 v146, v135
	s_mov_b64 s[46:47], 0x3a280000
	v_lshl_add_u64 v[150:151], v[74:75], 0, s[46:47]
	v_cvt_pk_bf16_f32 v135, v144, v145
	global_store_dword v[150:151], v135, off
	v_mov_b32_e32 v135, v134
	v_mov_b32_e32 v147, v146
	s_and_saveexec_b64 s[46:47], s[38:39]
	s_cbranch_execz .LBB0_839
	s_mov_b64 s[48:49], 0x24708800
	v_lshl_add_u64 v[148:149], v[76:77], 0, s[48:49]
	global_store_dwordx2 v[148:149], v[40:41], off nt
	s_and_saveexec_b64 s[48:49], s[40:41]
	s_cbranch_execz .LBB0_838
	v_lshl_add_u64 v[148:149], s[0:1], 0, v[6:7]
	v_add_co_u32_e32 v148, vcc, 0x24610000, v148
	s_nop 1
	v_addc_co_u32_e32 v149, vcc, 0, v149, vcc
	global_store_dword v[148:149], v154, off offset:272

.LBB0_839:
	s_or_b64 exec, exec, s[46:47]
	s_waitcnt vmcnt(25)
	v_lshlrev_b32_e32 v142, 16, v204
	v_and_b32_e32 v143, 0xffff0000, v204
	v_pk_mul_f32 v[142:143], v[146:147], v[142:143]
	v_add_f32_e32 v130, v130, v136
	v_max_f32_e32 v138, v131, v131
	v_pk_fma_f32 v[134:135], v[144:145], v[134:135], v[142:143]
	v_max_f32_e32 v144, v130, v138
	v_sub_f32_e32 v130, v130, v144
	v_sub_f32_e32 v131, v131, v144
	v_mul_f32_e32 v130, 0x3fb8aa3b, v130
	v_mul_f32_e32 v131, 0x3fb8aa3b, v131
	v_exp_f32_e32 v130, v130
	v_exp_f32_e32 v142, v131
	s_mov_b64 s[46:47], 0x3a300000
	v_lshl_add_u64 v[148:149], v[74:75], 0, s[46:47]
	v_cvt_pk_bf16_f32 v131, v134, v135
	global_store_dword v[148:149], v131, off
	v_mov_b32_e32 v131, v130
	v_mov_b32_e32 v143, v142
	s_and_saveexec_b64 s[46:47], s[38:39]
	s_cbranch_execz .LBB0_843
	s_mov_b64 s[48:49], 0x24709000
	v_lshl_add_u64 v[146:147], v[76:77], 0, s[48:49]
	global_store_dwordx2 v[146:147], v[40:41], off nt
	s_and_saveexec_b64 s[48:49], s[40:41]
	s_cbranch_execz .LBB0_842
	v_lshl_add_u64 v[146:147], s[0:1], 0, v[6:7]
	v_add_co_u32_e32 v146, vcc, 0x24610000, v146
	s_nop 1
	v_addc_co_u32_e32 v147, vcc, 0, v147, vcc
	global_store_dword v[146:147], v136, off offset:288

.LBB0_843:
	s_or_b64 exec, exec, s[46:47]
	v_lshlrev_b32_e32 v132, 16, v203
	v_and_b32_e32 v133, 0xffff0000, v203
	v_pk_mul_f32 v[132:133], v[142:143], v[132:133]
	v_add_f32_e32 v126, v126, v144
	v_pk_fma_f32 v[130:131], v[134:135], v[130:131], v[132:133]
	v_max_f32_e32 v132, v127, v127
	v_max_f32_e32 v134, v126, v132
	v_sub_f32_e32 v126, v126, v134
	v_sub_f32_e32 v127, v127, v134
	v_mul_f32_e32 v126, 0x3fb8aa3b, v126
	v_mul_f32_e32 v127, 0x3fb8aa3b, v127
	v_exp_f32_e32 v126, v126
	v_exp_f32_e32 v132, v127
	s_mov_b64 s[46:47], 0x3a380000
	v_lshl_add_u64 v[146:147], v[74:75], 0, s[46:47]
	v_cvt_pk_bf16_f32 v127, v130, v131
	global_store_dword v[146:147], v127, off
	v_mov_b32_e32 v127, v126
	v_mov_b32_e32 v133, v132
	s_and_saveexec_b64 s[46:47], s[38:39]
	s_cbranch_execz .LBB0_847
	s_mov_b64 s[48:49], 0x24709800
	v_lshl_add_u64 v[142:143], v[76:77], 0, s[48:49]
	global_store_dwordx2 v[142:143], v[40:41], off nt
	s_and_saveexec_b64 s[48:49], s[40:41]
	s_cbranch_execz .LBB0_846
	v_lshl_add_u64 v[142:143], s[0:1], 0, v[6:7]
	v_add_co_u32_e32 v142, vcc, 0x24610000, v142
	s_nop 1
	v_addc_co_u32_e32 v143, vcc, 0, v143, vcc
	global_store_dword v[142:143], v144, off offset:304

.LBB0_847:
	s_or_b64 exec, exec, s[46:47]
	v_lshlrev_b32_e32 v128, 16, v202
	v_and_b32_e32 v129, 0xffff0000, v202
	v_pk_mul_f32 v[128:129], v[132:133], v[128:129]
	v_add_f32_e32 v122, v122, v134
	v_pk_fma_f32 v[126:127], v[130:131], v[126:127], v[128:129]
	v_max_f32_e32 v128, v123, v123
	v_max_f32_e32 v130, v122, v128
	v_sub_f32_e32 v122, v122, v130
	v_sub_f32_e32 v123, v123, v130
	v_mul_f32_e32 v122, 0x3fb8aa3b, v122
	v_mul_f32_e32 v123, 0x3fb8aa3b, v123
	v_exp_f32_e32 v122, v122
	v_exp_f32_e32 v128, v123
	s_mov_b64 s[46:47], 0x3a400000
	v_lshl_add_u64 v[142:143], v[74:75], 0, s[46:47]
	v_cvt_pk_bf16_f32 v123, v126, v127
	global_store_dword v[142:143], v123, off
	v_mov_b32_e32 v123, v122
	v_mov_b32_e32 v129, v128
	s_and_saveexec_b64 s[46:47], s[38:39]
	s_cbranch_execz .LBB0_851
	s_mov_b64 s[48:49], 0x2470a000
	v_lshl_add_u64 v[132:133], v[76:77], 0, s[48:49]
	global_store_dwordx2 v[132:133], v[40:41], off nt
	s_and_saveexec_b64 s[48:49], s[40:41]
	s_cbranch_execz .LBB0_850
	v_lshl_add_u64 v[132:133], s[0:1], 0, v[6:7]
	v_add_co_u32_e32 v132, vcc, 0x24610000, v132
	s_nop 1
	v_addc_co_u32_e32 v133, vcc, 0, v133, vcc
	global_store_dword v[132:133], v134, off offset:320

.LBB0_851:
	s_or_b64 exec, exec, s[46:47]
	v_lshlrev_b32_e32 v124, 16, v185
	v_and_b32_e32 v125, 0xffff0000, v185
	v_pk_mul_f32 v[134:135], v[128:129], v[124:125]
	v_add_f32_e32 v118, v118, v130
	v_max_f32_e32 v124, v119, v119
	v_max_f32_e32 v128, v118, v124
	v_sub_f32_e32 v118, v118, v128
	v_sub_f32_e32 v119, v119, v128
	v_mul_f32_e32 v118, 0x3fb8aa3b, v118
	v_mul_f32_e32 v119, 0x3fb8aa3b, v119
	v_exp_f32_e32 v118, v118
	v_exp_f32_e32 v124, v119
	s_mov_b64 s[46:47], 0x3a480000
	v_pk_fma_f32 v[122:123], v[126:127], v[122:123], v[134:135]
	v_lshl_add_u64 v[132:133], v[74:75], 0, s[46:47]
	v_cvt_pk_bf16_f32 v119, v122, v123
	global_store_dword v[132:133], v119, off
	s_and_saveexec_b64 s[46:47], s[38:39]
	s_cbranch_execz .LBB0_855
	s_mov_b64 s[48:49], 0x2470a800
	v_lshl_add_u64 v[126:127], v[76:77], 0, s[48:49]
	global_store_dwordx2 v[126:127], v[40:41], off nt
	s_and_saveexec_b64 s[48:49], s[40:41]
	s_cbranch_execz .LBB0_854
	v_lshl_add_u64 v[126:127], s[0:1], 0, v[6:7]
	v_add_co_u32_e32 v126, vcc, 0x24610000, v126
	s_nop 1
	v_addc_co_u32_e32 v127, vcc, 0, v127, vcc
	global_store_dword v[126:127], v130, off offset:336

.LBB0_855:
	s_or_b64 exec, exec, s[46:47]
	s_waitcnt vmcnt(28)
	v_lshlrev_b32_e32 v120, 16, v184
	v_and_b32_e32 v121, 0xffff0000, v184
	v_pk_mul_f32 v[120:121], v[124:125], v[120:121] op_sel_hi:[0,1]
	v_pk_fma_f32 v[118:119], v[122:123], v[118:119], v[120:121] op_sel_hi:[1,0,1]
	v_add_f32_e32 v114, v114, v128
	v_max_f32_e32 v120, v115, v115
	v_max_f32_e32 v122, v114, v120
	v_sub_f32_e32 v114, v114, v122
	v_sub_f32_e32 v115, v115, v122
	v_mul_f32_e32 v114, 0x3fb8aa3b, v114
	v_mul_f32_e32 v115, 0x3fb8aa3b, v115
	v_exp_f32_e32 v114, v114
	v_exp_f32_e32 v120, v115
	s_mov_b64 s[46:47], 0x3a500000
	v_lshl_add_u64 v[126:127], v[74:75], 0, s[46:47]
	v_cvt_pk_bf16_f32 v115, v118, v119
	global_store_dword v[126:127], v115, off
	v_mov_b32_e32 v115, v114
	v_mov_b32_e32 v121, v120
	s_and_saveexec_b64 s[46:47], s[38:39]
	s_cbranch_execz .LBB0_859
	s_mov_b64 s[48:49], 0x2470b000
	v_lshl_add_u64 v[124:125], v[76:77], 0, s[48:49]
	global_store_dwordx2 v[124:125], v[40:41], off nt
	s_and_saveexec_b64 s[48:49], s[40:41]
	s_cbranch_execz .LBB0_858
	v_lshl_add_u64 v[124:125], s[0:1], 0, v[6:7]
	v_add_co_u32_e32 v124, vcc, 0x24610000, v124
	s_nop 1
	v_addc_co_u32_e32 v125, vcc, 0, v125, vcc
	global_store_dword v[124:125], v128, off offset:352

.LBB0_859:
	s_or_b64 exec, exec, s[46:47]
	v_lshlrev_b32_e32 v116, 16, v183
	v_and_b32_e32 v117, 0xffff0000, v183
	v_pk_mul_f32 v[116:117], v[120:121], v[116:117]
	v_add_f32_e32 v110, v110, v122
	v_pk_fma_f32 v[114:115], v[118:119], v[114:115], v[116:117]
	v_max_f32_e32 v116, v111, v111
	v_max_f32_e32 v118, v110, v116
	v_sub_f32_e32 v110, v110, v118
	v_sub_f32_e32 v111, v111, v118
	v_mul_f32_e32 v110, 0x3fb8aa3b, v110
	v_mul_f32_e32 v111, 0x3fb8aa3b, v111
	v_exp_f32_e32 v110, v110
	v_exp_f32_e32 v116, v111
	s_mov_b64 s[46:47], 0x3a580000
	v_lshl_add_u64 v[124:125], v[74:75], 0, s[46:47]
	v_cvt_pk_bf16_f32 v111, v114, v115
	global_store_dword v[124:125], v111, off
	v_mov_b32_e32 v111, v110
	v_mov_b32_e32 v117, v116
	s_and_saveexec_b64 s[46:47], s[38:39]
	s_cbranch_execz .LBB0_863
	s_mov_b64 s[48:49], 0x2470b800
	v_lshl_add_u64 v[120:121], v[76:77], 0, s[48:49]
	global_store_dwordx2 v[120:121], v[40:41], off nt
	s_and_saveexec_b64 s[48:49], s[40:41]
	s_cbranch_execz .LBB0_862
	v_lshl_add_u64 v[120:121], s[0:1], 0, v[6:7]
	v_add_co_u32_e32 v120, vcc, 0x24610000, v120
	s_nop 1
	v_addc_co_u32_e32 v121, vcc, 0, v121, vcc
	global_store_dword v[120:121], v122, off offset:368

.LBB0_863:
	s_or_b64 exec, exec, s[46:47]
	v_lshlrev_b32_e32 v112, 16, v182
	v_and_b32_e32 v113, 0xffff0000, v182
	v_pk_mul_f32 v[112:113], v[116:117], v[112:113]
	v_add_f32_e32 v106, v106, v118
	v_pk_fma_f32 v[110:111], v[114:115], v[110:111], v[112:113]
	v_max_f32_e32 v112, v107, v107
	v_max_f32_e32 v114, v106, v112
	v_sub_f32_e32 v106, v106, v114
	v_sub_f32_e32 v107, v107, v114
	v_mul_f32_e32 v106, 0x3fb8aa3b, v106
	v_mul_f32_e32 v107, 0x3fb8aa3b, v107
	v_exp_f32_e32 v106, v106
	v_exp_f32_e32 v112, v107
	s_mov_b64 s[46:47], 0x3a600000
	v_lshl_add_u64 v[120:121], v[74:75], 0, s[46:47]
	v_cvt_pk_bf16_f32 v107, v110, v111
	global_store_dword v[120:121], v107, off
	v_mov_b32_e32 v107, v106
	v_mov_b32_e32 v113, v112
	s_and_saveexec_b64 s[46:47], s[38:39]
	s_cbranch_execz .LBB0_867
	s_mov_b64 s[48:49], 0x2470c000
	v_lshl_add_u64 v[116:117], v[76:77], 0, s[48:49]
	global_store_dwordx2 v[116:117], v[40:41], off nt
	s_and_saveexec_b64 s[48:49], s[40:41]
	s_cbranch_execz .LBB0_866
	v_lshl_add_u64 v[116:117], s[0:1], 0, v[6:7]
	v_add_co_u32_e32 v116, vcc, 0x24610000, v116
	s_nop 1
	v_addc_co_u32_e32 v117, vcc, 0, v117, vcc
	global_store_dword v[116:117], v118, off offset:384

.LBB0_867:
	s_or_b64 exec, exec, s[46:47]
	v_lshlrev_b32_e32 v108, 16, v181
	v_and_b32_e32 v109, 0xffff0000, v181
	v_pk_mul_f32 v[108:109], v[112:113], v[108:109]
	v_add_f32_e32 v102, v102, v114
	v_pk_fma_f32 v[106:107], v[110:111], v[106:107], v[108:109]
	v_max_f32_e32 v108, v103, v103
	v_max_f32_e32 v110, v102, v108
	v_sub_f32_e32 v102, v102, v110
	v_sub_f32_e32 v103, v103, v110
	v_mul_f32_e32 v102, 0x3fb8aa3b, v102
	v_mul_f32_e32 v103, 0x3fb8aa3b, v103
	v_exp_f32_e32 v102, v102
	v_exp_f32_e32 v108, v103
	s_mov_b64 s[46:47], 0x3a680000
	v_lshl_add_u64 v[116:117], v[74:75], 0, s[46:47]
	v_cvt_pk_bf16_f32 v103, v106, v107
	global_store_dword v[116:117], v103, off
	v_mov_b32_e32 v103, v102
	v_mov_b32_e32 v109, v108
	s_and_saveexec_b64 s[46:47], s[38:39]
	s_cbranch_execz .LBB0_871
	s_mov_b64 s[48:49], 0x2470c800
	v_lshl_add_u64 v[112:113], v[76:77], 0, s[48:49]
	global_store_dwordx2 v[112:113], v[40:41], off nt
	s_and_saveexec_b64 s[48:49], s[40:41]
	s_cbranch_execz .LBB0_870
	v_lshl_add_u64 v[112:113], s[0:1], 0, v[6:7]
	v_add_co_u32_e32 v112, vcc, 0x24610000, v112
	s_nop 1
	v_addc_co_u32_e32 v113, vcc, 0, v113, vcc
	global_store_dword v[112:113], v114, off offset:400

.LBB0_871:
	s_or_b64 exec, exec, s[46:47]
	s_waitcnt vmcnt(31)
	v_lshlrev_b32_e32 v104, 16, v180
	v_and_b32_e32 v105, 0xffff0000, v180
	v_pk_mul_f32 v[114:115], v[108:109], v[104:105]
	v_add_f32_e32 v98, v98, v110
	v_max_f32_e32 v104, v99, v99
	v_max_f32_e32 v108, v98, v104
	v_sub_f32_e32 v98, v98, v108
	v_sub_f32_e32 v99, v99, v108
	v_mul_f32_e32 v98, 0x3fb8aa3b, v98
	v_mul_f32_e32 v99, 0x3fb8aa3b, v99
	v_exp_f32_e32 v98, v98
	v_exp_f32_e32 v104, v99
	s_mov_b64 s[46:47], 0x3a700000
	v_pk_fma_f32 v[102:103], v[106:107], v[102:103], v[114:115]
	v_lshl_add_u64 v[112:113], v[74:75], 0, s[46:47]
	v_cvt_pk_bf16_f32 v99, v102, v103
	global_store_dword v[112:113], v99, off
	s_and_saveexec_b64 s[46:47], s[38:39]
	s_cbranch_execz .LBB0_875
	s_mov_b64 s[48:49], 0x2470d000
	v_lshl_add_u64 v[106:107], v[76:77], 0, s[48:49]
	global_store_dwordx2 v[106:107], v[40:41], off nt
	s_and_saveexec_b64 s[48:49], s[40:41]
	s_cbranch_execz .LBB0_874
	v_lshl_add_u64 v[106:107], s[0:1], 0, v[6:7]
	v_add_co_u32_e32 v106, vcc, 0x24610000, v106
	s_nop 1
	v_addc_co_u32_e32 v107, vcc, 0, v107, vcc
	global_store_dword v[106:107], v110, off offset:416

.LBB0_875:
	s_or_b64 exec, exec, s[46:47]
	v_lshlrev_b32_e32 v100, 16, v179
	v_and_b32_e32 v101, 0xffff0000, v179
	v_pk_mul_f32 v[100:101], v[104:105], v[100:101] op_sel_hi:[0,1]
	v_pk_fma_f32 v[98:99], v[102:103], v[98:99], v[100:101] op_sel_hi:[1,0,1]
	v_add_f32_e32 v94, v94, v108
	v_max_f32_e32 v100, v95, v95
	v_max_f32_e32 v102, v94, v100
	v_sub_f32_e32 v94, v94, v102
	v_sub_f32_e32 v95, v95, v102
	v_mul_f32_e32 v94, 0x3fb8aa3b, v94
	v_mul_f32_e32 v95, 0x3fb8aa3b, v95
	v_exp_f32_e32 v94, v94
	v_exp_f32_e32 v100, v95
	s_mov_b64 s[46:47], 0x3a780000
	v_lshl_add_u64 v[106:107], v[74:75], 0, s[46:47]
	v_cvt_pk_bf16_f32 v95, v98, v99
	global_store_dword v[106:107], v95, off
	v_mov_b32_e32 v95, v94
	v_mov_b32_e32 v101, v100
	s_and_saveexec_b64 s[46:47], s[38:39]
	s_cbranch_execz .LBB0_879
	s_mov_b64 s[48:49], 0x2470d800
	v_lshl_add_u64 v[104:105], v[76:77], 0, s[48:49]
	global_store_dwordx2 v[104:105], v[40:41], off nt
	s_and_saveexec_b64 s[48:49], s[40:41]
	s_cbranch_execz .LBB0_878
	v_lshl_add_u64 v[104:105], s[0:1], 0, v[6:7]
	v_add_co_u32_e32 v104, vcc, 0x24610000, v104
	s_nop 1
	v_addc_co_u32_e32 v105, vcc, 0, v105, vcc
	global_store_dword v[104:105], v108, off offset:432

.LBB0_879:
	s_or_b64 exec, exec, s[46:47]
	s_waitcnt vmcnt(31)
	v_lshlrev_b32_e32 v96, 16, v178
	v_and_b32_e32 v97, 0xffff0000, v178
	v_pk_mul_f32 v[96:97], v[100:101], v[96:97]
	v_add_f32_e32 v90, v90, v102
	v_pk_fma_f32 v[94:95], v[98:99], v[94:95], v[96:97]
	v_max_f32_e32 v96, v91, v91
	v_max_f32_e32 v98, v90, v96
	v_sub_f32_e32 v90, v90, v98
	v_sub_f32_e32 v91, v91, v98
	v_mul_f32_e32 v90, 0x3fb8aa3b, v90
	v_mul_f32_e32 v91, 0x3fb8aa3b, v91
	v_exp_f32_e32 v90, v90
	v_exp_f32_e32 v96, v91
	s_mov_b64 s[46:47], 0x3a800000
	v_lshl_add_u64 v[104:105], v[74:75], 0, s[46:47]
	v_cvt_pk_bf16_f32 v91, v94, v95
	global_store_dword v[104:105], v91, off
	v_mov_b32_e32 v91, v90
	v_mov_b32_e32 v97, v96
	s_and_saveexec_b64 s[46:47], s[38:39]
	s_cbranch_execz .LBB0_883
	s_mov_b64 s[48:49], 0x2470e000
	v_lshl_add_u64 v[100:101], v[76:77], 0, s[48:49]
	global_store_dwordx2 v[100:101], v[40:41], off nt
	s_and_saveexec_b64 s[48:49], s[40:41]
	s_cbranch_execz .LBB0_882
	v_lshl_add_u64 v[100:101], s[0:1], 0, v[6:7]
	v_add_co_u32_e32 v100, vcc, 0x24610000, v100
	s_nop 1
	v_addc_co_u32_e32 v101, vcc, 0, v101, vcc
	global_store_dword v[100:101], v102, off offset:448

.LBB0_883:
	s_or_b64 exec, exec, s[46:47]
	s_waitcnt vmcnt(31)
	v_lshlrev_b32_e32 v92, 16, v177
	v_and_b32_e32 v93, 0xffff0000, v177
	v_pk_mul_f32 v[92:93], v[96:97], v[92:93]
	v_add_f32_e32 v86, v86, v98
	v_pk_fma_f32 v[90:91], v[94:95], v[90:91], v[92:93]
	v_max_f32_e32 v92, v87, v87
	v_max_f32_e32 v94, v86, v92
	v_sub_f32_e32 v86, v86, v94
	v_sub_f32_e32 v87, v87, v94
	v_mul_f32_e32 v86, 0x3fb8aa3b, v86
	v_mul_f32_e32 v87, 0x3fb8aa3b, v87
	v_exp_f32_e32 v86, v86
	v_exp_f32_e32 v92, v87
	s_mov_b64 s[46:47], 0x3a880000
	v_lshl_add_u64 v[100:101], v[74:75], 0, s[46:47]
	v_cvt_pk_bf16_f32 v87, v90, v91
	global_store_dword v[100:101], v87, off
	v_mov_b32_e32 v87, v86
	v_mov_b32_e32 v93, v92
	s_and_saveexec_b64 s[46:47], s[38:39]
	s_cbranch_execz .LBB0_887
	s_mov_b64 s[48:49], 0x2470e800
	v_lshl_add_u64 v[96:97], v[76:77], 0, s[48:49]
	global_store_dwordx2 v[96:97], v[40:41], off nt
	s_and_saveexec_b64 s[48:49], s[40:41]
	s_cbranch_execz .LBB0_886
	v_lshl_add_u64 v[96:97], s[0:1], 0, v[6:7]
	v_add_co_u32_e32 v96, vcc, 0x24610000, v96
	s_nop 1
	v_addc_co_u32_e32 v97, vcc, 0, v97, vcc
	global_store_dword v[96:97], v98, off offset:464

.LBB0_887:
	s_or_b64 exec, exec, s[46:47]
	v_lshlrev_b32_e32 v88, 16, v176
	v_and_b32_e32 v89, 0xffff0000, v176
	v_pk_mul_f32 v[88:89], v[92:93], v[88:89]
	v_add_f32_e32 v82, v82, v94
	v_pk_fma_f32 v[86:87], v[90:91], v[86:87], v[88:89]
	v_max_f32_e32 v88, v83, v83
	v_max_f32_e32 v90, v82, v88
	v_sub_f32_e32 v82, v82, v90
	v_sub_f32_e32 v83, v83, v90
	v_mul_f32_e32 v82, 0x3fb8aa3b, v82
	v_mul_f32_e32 v83, 0x3fb8aa3b, v83
	v_exp_f32_e32 v82, v82
	v_exp_f32_e32 v88, v83
	s_mov_b64 s[46:47], 0x3a900000
	v_lshl_add_u64 v[96:97], v[74:75], 0, s[46:47]
	v_cvt_pk_bf16_f32 v83, v86, v87
	global_store_dword v[96:97], v83, off
	v_mov_b32_e32 v83, v82
	v_mov_b32_e32 v89, v88
	s_and_saveexec_b64 s[46:47], s[38:39]
	s_cbranch_execz .LBB0_891
	s_mov_b64 s[48:49], 0x2470f000
	v_lshl_add_u64 v[92:93], v[76:77], 0, s[48:49]
	global_store_dwordx2 v[92:93], v[40:41], off nt
	s_and_saveexec_b64 s[48:49], s[40:41]
	s_cbranch_execz .LBB0_890
	v_lshl_add_u64 v[92:93], s[0:1], 0, v[6:7]
	v_add_co_u32_e32 v92, vcc, 0x24610000, v92
	s_nop 1
	v_addc_co_u32_e32 v93, vcc, 0, v93, vcc
	global_store_dword v[92:93], v94, off offset:480

.LBB0_891:
	s_or_b64 exec, exec, s[46:47]
	s_mov_b64 s[46:47], 0x3a980000
	s_waitcnt vmcnt(32)
	v_lshl_add_u64 v[84:85], v[74:75], 0, s[46:47]
	v_lshlrev_b32_e32 v74, 16, v175
	v_and_b32_e32 v75, 0xffff0000, v175
	v_pk_mul_f32 v[74:75], v[88:89], v[74:75]
	v_add_f32_e32 v78, v78, v90
	v_pk_fma_f32 v[74:75], v[86:87], v[82:83], v[74:75]
	v_max_f32_e32 v82, v79, v79
	v_max_f32_e32 v207, v78, v82
	v_sub_f32_e32 v78, v78, v207
	v_sub_f32_e32 v79, v79, v207
	v_mul_f32_e32 v78, 0x3fb8aa3b, v78
	v_mul_f32_e32 v79, 0x3fb8aa3b, v79
	v_exp_f32_e32 v78, v78
	v_exp_f32_e32 v82, v79
	v_cvt_pk_bf16_f32 v79, v74, v75
	global_store_dword v[84:85], v79, off
	v_mov_b32_e32 v79, v78
	v_mov_b32_e32 v83, v82
	s_and_saveexec_b64 s[46:47], s[38:39]
	s_cbranch_execz .LBB0_764
	s_mov_b64 s[48:49], 0x2470f800
	v_lshl_add_u64 v[76:77], v[76:77], 0, s[48:49]
	global_store_dwordx2 v[76:77], v[40:41], off nt
	s_and_saveexec_b64 s[48:49], s[40:41]
	s_cbranch_execz .LBB0_763
	v_lshl_add_u64 v[76:77], s[0:1], 0, v[6:7]
	v_add_co_u32_e32 v76, vcc, 0x24610000, v76
	s_nop 1
	v_addc_co_u32_e32 v77, vcc, 0, v77, vcc
	global_store_dword v[76:77], v90, off offset:496
	s_branch .LBB0_763
